# v57 + layer-1 combine/rmsnorm row loop and final norm row loop restructured: next row's routing record requested a row ahead, all expert-output chunk loads issued together, gain vector loaded once per
# speedup vs baseline: 1.0163x; 1.0027x over previous
.LBB0_2269:
	s_lshl_b32 s0, s0, 3
	s_add_i32 s2, s20, s0
	s_cmpk_gt_i32 s2, 0x3fff
	v_readlane_b32 s22, v254, 29
	s_mov_b32 s21, 0x38400000
	s_waitcnt lgkmcnt(0)
	s_barrier
	v_readlane_b32 s23, v254, 30
	s_cbranch_scc1 .LBB0_2272
	v_xor_b32_e32 v2, 1, v218
	v_cmp_lt_i32_e32 vcc, v2, v219
	s_load_dwordx2 s[4:5], s[10:11], 0x18
	v_lshlrev_b32_e32 v0, 5, v34
	v_cndmask_b32_e32 v2, v218, v2, vcc
	v_lshlrev_b32_e32 v35, 2, v2
	v_xor_b32_e32 v2, 2, v218
	v_cmp_lt_i32_e32 vcc, v2, v219
	s_waitcnt lgkmcnt(0)
	s_add_u32 s4, s4, 0x2000
	s_addc_u32 s5, s5, 0
	v_cndmask_b32_e32 v2, v218, v2, vcc
	v_lshlrev_b32_e32 v36, 2, v2
	v_xor_b32_e32 v2, 4, v218
	v_cmp_lt_i32_e32 vcc, v2, v219
	v_or_b32_e32 v4, 0x800, v0
	v_or_b32_e32 v6, 0x1000, v0
	v_cndmask_b32_e32 v2, v218, v2, vcc
	v_lshlrev_b32_e32 v37, 2, v2
	v_xor_b32_e32 v2, 8, v218
	v_cmp_lt_i32_e32 vcc, v2, v219
	s_ashr_i32 s3, s2, 31
	v_mov_b32_e32 v5, v1
	v_cndmask_b32_e32 v2, v218, v2, vcc
	v_lshlrev_b32_e32 v38, 2, v2
	v_xor_b32_e32 v2, 16, v218
	v_cmp_lt_i32_e32 vcc, v2, v219
	v_mov_b32_e32 v7, v1
	s_lshl_b64 s[6:7], s[2:3], 12
	v_cndmask_b32_e32 v2, v218, v2, vcc
	v_lshlrev_b32_e32 v39, 2, v2
	v_xor_b32_e32 v2, 32, v218
	v_cmp_lt_i32_e32 vcc, v2, v219
	v_lshl_add_u64 v[4:5], s[4:5], 0, v[4:5]
	v_lshl_add_u64 v[6:7], s[4:5], 0, v[6:7]
	v_cndmask_b32_e32 v2, v218, v2, vcc
	v_lshlrev_b32_e32 v40, 2, v2
	v_lshl_add_u64 v[2:3], s[4:5], 0, v[0:1]
	v_or_b32_e32 v0, 0x1800, v0
	v_lshl_add_u64 v[8:9], s[4:5], 0, v[0:1]
	v_lshlrev_b32_e32 v0, 4, v34
	v_lshl_add_u64 v[10:11], s[12:13], 0, v[0:1]
	s_mov_b64 s[4:5], 0x22600000
	s_add_u32 s0, s6, 0x1de00000
	v_lshlrev_b32_e32 v0, 4, v128
	v_lshl_add_u64 v[10:11], v[10:11], 0, s[4:5]
	s_addc_u32 s4, s7, 0
	v_and_b32_e32 v0, 0x3f0, v0
	v_mov_b32_e32 v13, s4
	s_lshl_b64 s[4:5], s[2:3], 4
	s_lshl_b64 s[14:15], s[2:3], 11
	v_or_b32_e32 v16, s6, v0
	v_mov_b32_e32 v17, s7
	s_lshl_b64 s[6:7], s[2:3], 3
	v_or_b32_e32 v12, s0, v0
	s_add_u32 s0, s6, 0x15d80000
	v_lshl_or_b32 v14, v34, 3, s14
	v_mov_b32_e32 v15, s15
	s_addc_u32 s3, s7, 0
	s_mov_b32 s14, s2
	v_mov_b32_e32 v250, 0x15d00000
	s_add_u32 s98, s12, s4
	s_addc_u32 s99, s13, s5
	global_load_dwordx4 v[246:249], v250, s[98:99]
	global_load_dwordx4 v[156:159], v[2:3], off
	global_load_dwordx4 v[160:163], v[2:3], off offset:16
	global_load_dwordx4 v[164:167], v[4:5], off
	global_load_dwordx4 v[168:171], v[4:5], off offset:16
	global_load_dwordx4 v[172:175], v[6:7], off
	global_load_dwordx4 v[176:179], v[6:7], off offset:16
	global_load_dwordx4 v[180:183], v[8:9], off
	global_load_dwordx4 v[184:187], v[8:9], off offset:16
	s_waitcnt vmcnt(0)
.LBB0_2271:
	v_lshl_add_u64 v[20:21], s[12:13], 0, v[16:17]
	s_mov_b32 s15, 0x15e00000
	v_add_co_u32_e32 v32, vcc, s15, v20
	v_lshl_add_u64 v[24:25], s[12:13], 0, v[14:15]
	v_addc_co_u32_e32 v33, vcc, 0, v21, vcc
	v_add_co_u32_e32 v20, vcc, s21, v24
	s_nop 0
	v_addc_co_u32_e32 v21, vcc, 0, v25, vcc
	s_add_u32 s6, s12, s0
	s_addc_u32 s7, s13, s3
	s_add_i32 s15, 0, 0x20200
	v_mov_b32_e32 v22, v1
	v_mov_b32_e32 v23, v1
	v_lshl_add_u64 v[18:19], s[12:13], 0, v[12:13]
	s_add_i32 s14, s14, s22
	v_lshl_add_u64 v[12:13], v[12:13], 0, s[74:75]
	v_lshl_add_u64 v[14:15], v[14:15], 0, s[66:67]
	v_lshl_add_u64 v[16:17], v[16:17], 0, s[74:75]
	v_readfirstlane_b32 s16, v246
	v_readfirstlane_b32 s18, v248
	s_lshl_b32 s16, s16, 2
	s_lshl_b32 s18, s18, 2
	s_add_i32 s16, s15, s16
	s_add_i32 s15, s15, s18
	v_mov_b32_e32 v0, s16
	v_mov_b32_e32 v24, s15
	ds_read_b32 v0, v0
	ds_read_b32 v41, v24
	v_readfirstlane_b32 s17, v247
	v_readfirstlane_b32 s19, v249
	s_add_u32 s98, s4, s80
	s_addc_u32 s99, s5, s81
	s_add_u32 s98, s98, s12
	s_addc_u32 s99, s99, s13
	global_load_dwordx4 v[246:249], v250, s[98:99]
	global_load_dwordx4 v[24:27], v[32:33], off
	global_load_dwordx4 v[28:31], v[32:33], off offset:1024
	global_load_dwordx4 v[42:45], v[32:33], off offset:2048
	global_load_dwordx2 v[58:59], v1, s[6:7]
	global_load_dwordx4 v[46:49], v[32:33], off offset:3072
	s_waitcnt lgkmcnt(1)
	v_readfirstlane_b32 s6, v0
	s_waitcnt lgkmcnt(0)
	v_readfirstlane_b32 s7, v41
	s_lshl_b32 s7, s7, 8
	s_lshl_b32 s6, s6, 8
	s_add_i32 s16, s7, s19
	s_add_i32 s6, s6, s17
	s_ashr_i32 s17, s16, 31
	s_ashr_i32 s7, s6, 31
	s_lshl_b64 s[16:17], s[16:17], 12
	s_lshl_b64 s[6:7], s[6:7], 12
	v_lshl_add_u64 v[62:63], v[10:11], 0, s[16:17]
	v_lshl_add_u64 v[60:61], v[10:11], 0, s[6:7]
	global_load_dwordx4 v[50:53], v[62:63], off
	global_load_dwordx4 v[54:57], v[60:61], off
	global_load_dwordx4 v[198:201], v[62:63], off offset:1024
	global_load_dwordx4 v[202:205], v[60:61], off offset:1024
	global_load_dwordx4 v[206:209], v[62:63], off offset:2048
	global_load_dwordx4 v[210:213], v[60:61], off offset:2048
	global_load_dwordx4 v[214:217], v[62:63], off offset:3072
	global_load_dwordx4 v[242:245], v[60:61], off offset:3072
	s_add_u32 s4, s4, s80
	s_addc_u32 s5, s5, s81
	s_add_u32 s0, s0, s84
	s_addc_u32 s3, s3, s85
	s_cmpk_gt_i32 s14, 0x3fff
	s_waitcnt vmcnt(12)
	v_lshlrev_b32_e32 v64, 16, v27
	v_and_b32_e32 v65, 0xffff0000, v27
	v_lshlrev_b32_e32 v68, 16, v26
	v_and_b32_e32 v69, 0xffff0000, v26
	s_waitcnt vmcnt(11)
	v_lshlrev_b32_e32 v70, 16, v28
	v_and_b32_e32 v71, 0xffff0000, v28
	v_lshlrev_b32_e32 v72, 16, v29
	v_and_b32_e32 v73, 0xffff0000, v29
	v_lshlrev_b32_e32 v74, 16, v30
	v_and_b32_e32 v75, 0xffff0000, v30
	v_lshlrev_b32_e32 v76, 16, v31
	v_and_b32_e32 v77, 0xffff0000, v31
	v_lshlrev_b32_e32 v66, 16, v24
	v_and_b32_e32 v67, 0xffff0000, v24
	v_lshlrev_b32_e32 v24, 16, v25
	v_and_b32_e32 v25, 0xffff0000, v25
	s_waitcnt vmcnt(7)
	v_lshlrev_b32_e32 v26, 16, v50
	s_waitcnt vmcnt(6)
	v_and_b32_e32 v27, 0xffff0000, v54
	v_lshlrev_b32_e32 v28, 16, v54
	v_and_b32_e32 v29, 0xffff0000, v50
	v_lshlrev_b32_e32 v30, 16, v51
	v_lshlrev_b32_e32 v50, 16, v55
	v_and_b32_e32 v51, 0xffff0000, v51
	v_lshlrev_b32_e32 v54, 16, v52
	v_lshlrev_b32_e32 v86, 16, v56
	v_and_b32_e32 v87, 0xffff0000, v52
	v_lshlrev_b32_e32 v88, 16, v53
	v_lshlrev_b32_e32 v52, 16, v57
	v_and_b32_e32 v53, 0xffff0000, v53
	v_and_b32_e32 v31, 0xffff0000, v55
	v_and_b32_e32 v55, 0xffff0000, v56
	v_and_b32_e32 v89, 0xffff0000, v57
	v_pk_mul_f32 v[28:29], v[58:59], v[28:29]
	v_pk_mul_f32 v[50:51], v[58:59], v[50:51]
	v_pk_mul_f32 v[56:57], v[58:59], v[86:87]
	v_pk_mul_f32 v[52:53], v[58:59], v[52:53]
	v_pk_fma_f32 v[26:27], v[58:59], v[26:27], v[28:29] op_sel:[1,0,0] op_sel_hi:[0,1,1]
	v_pk_fma_f32 v[28:29], v[58:59], v[30:31], v[50:51] op_sel:[1,0,0] op_sel_hi:[0,1,1]
	v_pk_fma_f32 v[30:31], v[58:59], v[54:55], v[56:57] op_sel:[1,0,0] op_sel_hi:[0,1,1]
	v_pk_fma_f32 v[50:51], v[58:59], v[88:89], v[52:53] op_sel:[1,0,0] op_sel_hi:[0,1,1]
	v_pk_add_f32 v[52:53], v[26:27], v[66:67]
	v_pk_add_f32 v[54:55], v[28:29], v[24:25]
	v_pk_add_f32 v[56:57], v[30:31], v[68:69]
	v_pk_add_f32 v[50:51], v[50:51], v[64:65]
	v_cvt_pk_bf16_f32 v24, v52, v53
	v_cvt_pk_bf16_f32 v25, v54, v55
	v_cvt_pk_bf16_f32 v26, v56, v57
	v_cvt_pk_bf16_f32 v27, v50, v51
	v_pk_mul_f32 v[28:29], v[52:53], v[52:53]
	v_pk_mul_f32 v[30:31], v[54:55], v[54:55]
	v_pk_mul_f32 v[66:67], v[50:51], v[50:51]
	global_store_dwordx4 v[32:33], v[24:27], off
	v_add_f32_e32 v0, v66, v67
	v_add_f32_e32 v41, v30, v31
	v_add_f32_e32 v66, v28, v29
	v_pk_mul_f32 v[64:65], v[56:57], v[56:57]
	v_add_f32_e32 v41, v66, v41
	v_add_f32_e32 v64, v64, v65
	v_add_f32_e32 v41, v64, v41
	v_add_f32_e32 v0, v0, v41
	v_lshlrev_b32_e32 v78, 16, v42
	v_and_b32_e32 v79, 0xffff0000, v42
	v_lshlrev_b32_e32 v42, 16, v43
	v_and_b32_e32 v43, 0xffff0000, v43
	v_lshlrev_b32_e32 v80, 16, v44
	v_and_b32_e32 v81, 0xffff0000, v44
	v_lshlrev_b32_e32 v44, 16, v45
	v_and_b32_e32 v45, 0xffff0000, v45
	v_lshlrev_b32_e32 v82, 16, v46
	v_and_b32_e32 v83, 0xffff0000, v46
	v_lshlrev_b32_e32 v46, 16, v47
	v_and_b32_e32 v47, 0xffff0000, v47
	v_lshlrev_b32_e32 v84, 16, v48
	v_and_b32_e32 v85, 0xffff0000, v48
	v_lshlrev_b32_e32 v48, 16, v49
	v_and_b32_e32 v49, 0xffff0000, v49
	s_waitcnt vmcnt(5)
	v_lshlrev_b32_e32 v64, 16, v198
	s_waitcnt vmcnt(4)
	v_and_b32_e32 v65, 0xffff0000, v202
	v_lshlrev_b32_e32 v66, 16, v202
	v_and_b32_e32 v67, 0xffff0000, v198
	v_lshlrev_b32_e32 v68, 16, v199
	v_lshlrev_b32_e32 v24, 16, v203
	v_and_b32_e32 v25, 0xffff0000, v199
	v_lshlrev_b32_e32 v28, 16, v200
	v_lshlrev_b32_e32 v86, 16, v204
	v_and_b32_e32 v87, 0xffff0000, v200
	v_lshlrev_b32_e32 v88, 16, v201
	v_lshlrev_b32_e32 v26, 16, v205
	v_and_b32_e32 v27, 0xffff0000, v201
	v_and_b32_e32 v69, 0xffff0000, v203
	v_and_b32_e32 v29, 0xffff0000, v204
	v_and_b32_e32 v89, 0xffff0000, v205
	v_pk_mul_f32 v[30:31], v[58:59], v[66:67]
	v_pk_mul_f32 v[24:25], v[58:59], v[24:25]
	v_pk_mul_f32 v[66:67], v[58:59], v[86:87]
	v_pk_mul_f32 v[26:27], v[58:59], v[26:27]
	v_pk_fma_f32 v[30:31], v[58:59], v[64:65], v[30:31] op_sel:[1,0,0] op_sel_hi:[0,1,1]
	v_pk_fma_f32 v[24:25], v[58:59], v[68:69], v[24:25] op_sel:[1,0,0] op_sel_hi:[0,1,1]
	v_pk_fma_f32 v[28:29], v[58:59], v[28:29], v[66:67] op_sel:[1,0,0] op_sel_hi:[0,1,1]
	v_pk_fma_f32 v[26:27], v[58:59], v[88:89], v[26:27] op_sel:[1,0,0] op_sel_hi:[0,1,1]
	v_pk_add_f32 v[64:65], v[30:31], v[70:71]
	v_pk_add_f32 v[66:67], v[24:25], v[72:73]
	v_pk_add_f32 v[68:69], v[28:29], v[74:75]
	v_pk_add_f32 v[70:71], v[26:27], v[76:77]
	v_cvt_pk_bf16_f32 v24, v64, v65
	v_cvt_pk_bf16_f32 v25, v66, v67
	v_cvt_pk_bf16_f32 v26, v68, v69
	v_cvt_pk_bf16_f32 v27, v70, v71
	v_pk_mul_f32 v[28:29], v[64:65], v[64:65]
	v_pk_mul_f32 v[30:31], v[66:67], v[66:67]
	global_store_dwordx4 v[32:33], v[24:27], off offset:1024
	v_add_f32_e32 v41, v28, v29
	v_add_f32_e32 v76, v30, v31
	v_pk_mul_f32 v[72:73], v[68:69], v[68:69]
	v_add_f32_e32 v0, v0, v41
	v_pk_mul_f32 v[74:75], v[70:71], v[70:71]
	v_add_f32_e32 v72, v72, v73
	v_add_f32_e32 v0, v76, v0
	v_add_f32_e32 v73, v74, v75
	v_add_f32_e32 v0, v72, v0
	v_add_f32_e32 v0, v73, v0
	s_waitcnt vmcnt(3)
	v_lshlrev_b32_e32 v72, 16, v206
	s_waitcnt vmcnt(2)
	v_and_b32_e32 v73, 0xffff0000, v210
	v_lshlrev_b32_e32 v74, 16, v210
	v_and_b32_e32 v75, 0xffff0000, v206
	v_lshlrev_b32_e32 v76, 16, v207
	v_lshlrev_b32_e32 v24, 16, v211
	v_and_b32_e32 v25, 0xffff0000, v207
	v_lshlrev_b32_e32 v28, 16, v208
	v_lshlrev_b32_e32 v86, 16, v212
	v_and_b32_e32 v87, 0xffff0000, v208
	v_lshlrev_b32_e32 v88, 16, v209
	v_lshlrev_b32_e32 v26, 16, v213
	v_and_b32_e32 v27, 0xffff0000, v209
	v_and_b32_e32 v77, 0xffff0000, v211
	v_and_b32_e32 v29, 0xffff0000, v212
	v_and_b32_e32 v89, 0xffff0000, v213
	v_pk_mul_f32 v[30:31], v[58:59], v[74:75]
	v_pk_mul_f32 v[24:25], v[58:59], v[24:25]
	v_pk_mul_f32 v[74:75], v[58:59], v[86:87]
	v_pk_mul_f32 v[26:27], v[58:59], v[26:27]
	v_pk_fma_f32 v[30:31], v[58:59], v[72:73], v[30:31] op_sel:[1,0,0] op_sel_hi:[0,1,1]
	v_pk_fma_f32 v[24:25], v[58:59], v[76:77], v[24:25] op_sel:[1,0,0] op_sel_hi:[0,1,1]
	v_pk_fma_f32 v[28:29], v[58:59], v[28:29], v[74:75] op_sel:[1,0,0] op_sel_hi:[0,1,1]
	v_pk_fma_f32 v[26:27], v[58:59], v[88:89], v[26:27] op_sel:[1,0,0] op_sel_hi:[0,1,1]
	v_pk_add_f32 v[72:73], v[30:31], v[78:79]
	v_pk_add_f32 v[74:75], v[24:25], v[42:43]
	v_pk_add_f32 v[76:77], v[28:29], v[80:81]
	v_pk_add_f32 v[78:79], v[26:27], v[44:45]
	v_cvt_pk_bf16_f32 v24, v72, v73
	v_cvt_pk_bf16_f32 v25, v74, v75
	v_cvt_pk_bf16_f32 v26, v76, v77
	v_cvt_pk_bf16_f32 v27, v78, v79
	v_pk_mul_f32 v[28:29], v[72:73], v[72:73]
	v_pk_mul_f32 v[30:31], v[74:75], v[74:75]
	global_store_dwordx4 v[32:33], v[24:27], off offset:2048
	v_add_f32_e32 v41, v28, v29
	v_add_f32_e32 v80, v30, v31
	v_pk_mul_f32 v[42:43], v[76:77], v[76:77]
	v_add_f32_e32 v0, v0, v41
	v_pk_mul_f32 v[44:45], v[78:79], v[78:79]
	v_add_f32_e32 v42, v42, v43
	v_add_f32_e32 v0, v80, v0
	v_add_f32_e32 v43, v44, v45
	v_add_f32_e32 v0, v42, v0
	v_add_f32_e32 v0, v43, v0
	s_waitcnt vmcnt(1)
	v_lshlrev_b32_e32 v42, 16, v214
	s_waitcnt vmcnt(0)
	v_and_b32_e32 v43, 0xffff0000, v242
	v_lshlrev_b32_e32 v44, 16, v242
	v_and_b32_e32 v45, 0xffff0000, v214
	v_lshlrev_b32_e32 v60, 16, v215
	v_lshlrev_b32_e32 v24, 16, v243
	v_and_b32_e32 v25, 0xffff0000, v215
	v_lshlrev_b32_e32 v28, 16, v216
	v_lshlrev_b32_e32 v62, 16, v244
	v_and_b32_e32 v63, 0xffff0000, v216
	v_lshlrev_b32_e32 v80, 16, v217
	v_lshlrev_b32_e32 v26, 16, v245
	v_and_b32_e32 v27, 0xffff0000, v217
	v_and_b32_e32 v61, 0xffff0000, v243
	v_and_b32_e32 v29, 0xffff0000, v244
	v_and_b32_e32 v81, 0xffff0000, v245
	v_pk_mul_f32 v[30:31], v[58:59], v[44:45]
	v_pk_mul_f32 v[24:25], v[58:59], v[24:25]
	v_pk_mul_f32 v[44:45], v[58:59], v[62:63]
	v_pk_mul_f32 v[26:27], v[58:59], v[26:27]
	v_pk_fma_f32 v[30:31], v[58:59], v[42:43], v[30:31] op_sel:[1,0,0] op_sel_hi:[0,1,1]
	v_pk_fma_f32 v[24:25], v[58:59], v[60:61], v[24:25] op_sel:[1,0,0] op_sel_hi:[0,1,1]
	v_pk_fma_f32 v[28:29], v[58:59], v[28:29], v[44:45] op_sel:[1,0,0] op_sel_hi:[0,1,1]
	v_pk_fma_f32 v[42:43], v[58:59], v[80:81], v[26:27] op_sel:[1,0,0] op_sel_hi:[0,1,1]
	v_pk_add_f32 v[26:27], v[30:31], v[82:83]
	v_pk_add_f32 v[24:25], v[24:25], v[46:47]
	v_pk_add_f32 v[30:31], v[28:29], v[84:85]
	v_pk_add_f32 v[28:29], v[42:43], v[48:49]
	v_cvt_pk_bf16_f32 v42, v26, v27
	v_cvt_pk_bf16_f32 v43, v24, v25
	v_cvt_pk_bf16_f32 v44, v30, v31
	v_cvt_pk_bf16_f32 v45, v28, v29
	v_mov_b32_e32 v46, v25
	v_mov_b32_e32 v47, v27
	v_mov_b32_e32 v48, v29
	v_mov_b32_e32 v49, v31
	global_store_dwordx4 v[32:33], v[42:45], off offset:3072
	v_pk_mul_f32 v[32:33], v[46:47], v[46:47]
	v_pk_mul_f32 v[62:63], v[48:49], v[48:49]
	v_mov_b32_e32 v58, v24
	v_mov_b32_e32 v59, v26
	v_pk_fma_f32 v[32:33], v[58:59], v[58:59], v[32:33]
	v_mov_b32_e32 v60, v28
	v_mov_b32_e32 v61, v30
	v_add_f32_e32 v0, v0, v33
	v_pk_fma_f32 v[58:59], v[60:61], v[60:61], v[62:63]
	v_add_f32_e32 v0, v32, v0
	v_add_f32_e32 v0, v59, v0
	v_add_f32_e32 v0, v58, v0
	ds_bpermute_b32 v32, v35, v0
	s_waitcnt lgkmcnt(0)
	v_add_f32_e32 v0, v0, v32
	ds_bpermute_b32 v32, v36, v0
	s_waitcnt lgkmcnt(0)
	v_add_f32_e32 v0, v0, v32
	ds_bpermute_b32 v32, v37, v0
	s_waitcnt lgkmcnt(0)
	v_add_f32_e32 v0, v0, v32
	ds_bpermute_b32 v32, v38, v0
	s_waitcnt lgkmcnt(0)
	v_add_f32_e32 v0, v0, v32
	ds_bpermute_b32 v32, v39, v0
	s_waitcnt lgkmcnt(0)
	v_add_f32_e32 v0, v0, v32
	ds_bpermute_b32 v32, v40, v0
	s_waitcnt lgkmcnt(0)
	v_add_f32_e32 v0, v0, v32
	v_fmamk_f32 v0, v0, 0x3a000000, v220
	v_mul_f32_e32 v32, 0x4b800000, v0
	v_cmp_gt_f32_e32 vcc, s65, v0
	s_nop 1
	v_cndmask_b32_e32 v0, v0, v32, vcc
	v_rsq_f32_e32 v0, v0
	s_nop 0
	v_mul_f32_e32 v32, 0x45800000, v0
	v_cndmask_b32_e32 v0, v0, v32, vcc
	v_pk_mul_f32 v[32:33], v[52:53], v[0:1] op_sel_hi:[1,0]
	v_pk_mul_f32 v[52:53], v[56:57], v[0:1] op_sel_hi:[1,0]
	v_pk_mul_f32 v[54:55], v[54:55], v[0:1] op_sel_hi:[1,0]
	v_pk_mul_f32 v[50:51], v[50:51], v[0:1] op_sel_hi:[1,0]
	v_pk_mul_f32 v[24:25], v[24:25], v[0:1] op_sel_hi:[1,0]
	v_pk_mul_f32 v[28:29], v[28:29], v[0:1] op_sel_hi:[1,0]
	v_pk_mul_f32 v[32:33], v[156:157], v[32:33]
	v_pk_mul_f32 v[46:47], v[160:161], v[52:53]
	v_pk_mul_f32 v[44:45], v[158:159], v[54:55]
	v_pk_mul_f32 v[48:49], v[162:163], v[50:51]
	v_mul_f32_e32 v41, 0x42000000, v32
	v_mul_f32_e32 v50, 0x42000000, v33
	v_mul_f32_e32 v53, 0x42000000, v46
	v_mul_f32_e32 v54, 0x42000000, v47
	v_mul_f32_e32 v51, 0x42000000, v44
	v_mul_f32_e32 v52, 0x42000000, v45
	v_mul_f32_e32 v55, 0x42000000, v48
	v_cvt_pk_bf16_f32 v42, v32, v33
	v_cvt_pk_bf16_f32 v43, v44, v45
	v_cvt_pk_bf16_f32 v44, v46, v47
	v_cvt_pk_bf16_f32 v45, v48, v49
	v_med3_f32 v32, v41, s76, v237
	v_med3_f32 v33, v50, s76, v237
	v_med3_f32 v47, v53, s76, v237
	v_med3_f32 v48, v54, s76, v237
	v_cvt_pk_fp8_f32 v22, v32, v33
	v_cvt_pk_fp8_f32 v23, v47, v48
	v_mul_f32_e32 v56, 0x42000000, v49
	v_med3_f32 v41, v51, s76, v237
	v_med3_f32 v46, v52, s76, v237
	v_med3_f32 v49, v55, s76, v237
	v_med3_f32 v50, v56, s76, v237
	v_cvt_pk_fp8_f32 v22, v41, v46 op_sel:[0,0,1]
	v_cvt_pk_fp8_f32 v23, v49, v50 op_sel:[0,0,1]
	global_store_dwordx2 v[20:21], v[22:23], off
	global_store_dwordx4 v[18:19], v[42:45], off
	v_pk_mul_f32 v[32:33], v[64:65], v[0:1] op_sel_hi:[1,0]
	v_pk_mul_f32 v[50:51], v[68:69], v[0:1] op_sel_hi:[1,0]
	v_pk_mul_f32 v[52:53], v[66:67], v[0:1] op_sel_hi:[1,0]
	v_pk_mul_f32 v[54:55], v[70:71], v[0:1] op_sel_hi:[1,0]
	v_mov_b32_e32 v22, v1
	v_mov_b32_e32 v23, v1
	v_pk_mul_f32 v[32:33], v[164:165], v[32:33]
	v_pk_mul_f32 v[46:47], v[168:169], v[50:51]
	v_pk_mul_f32 v[44:45], v[166:167], v[52:53]
	v_pk_mul_f32 v[48:49], v[170:171], v[54:55]
	v_mul_f32_e32 v41, 0x42000000, v32
	v_mul_f32_e32 v50, 0x42000000, v33
	v_mul_f32_e32 v53, 0x42000000, v46
	v_mul_f32_e32 v54, 0x42000000, v47
	v_mul_f32_e32 v51, 0x42000000, v44
	v_mul_f32_e32 v52, 0x42000000, v45
	v_mul_f32_e32 v55, 0x42000000, v48
	v_cvt_pk_bf16_f32 v42, v32, v33
	v_cvt_pk_bf16_f32 v43, v44, v45
	v_cvt_pk_bf16_f32 v44, v46, v47
	v_cvt_pk_bf16_f32 v45, v48, v49
	v_med3_f32 v32, v41, s76, v237
	v_med3_f32 v33, v50, s76, v237
	v_med3_f32 v47, v53, s76, v237
	v_med3_f32 v48, v54, s76, v237
	v_cvt_pk_fp8_f32 v22, v32, v33
	v_cvt_pk_fp8_f32 v23, v47, v48
	v_mul_f32_e32 v56, 0x42000000, v49
	v_med3_f32 v41, v51, s76, v237
	v_med3_f32 v46, v52, s76, v237
	v_med3_f32 v49, v55, s76, v237
	v_med3_f32 v50, v56, s76, v237
	v_cvt_pk_fp8_f32 v22, v41, v46 op_sel:[0,0,1]
	v_cvt_pk_fp8_f32 v23, v49, v50 op_sel:[0,0,1]
	global_store_dwordx2 v[20:21], v[22:23], off offset:512
	global_store_dwordx4 v[18:19], v[42:45], off offset:1024
	v_pk_mul_f32 v[32:33], v[72:73], v[0:1] op_sel_hi:[1,0]
	v_pk_mul_f32 v[50:51], v[76:77], v[0:1] op_sel_hi:[1,0]
	v_pk_mul_f32 v[52:53], v[74:75], v[0:1] op_sel_hi:[1,0]
	v_pk_mul_f32 v[54:55], v[78:79], v[0:1] op_sel_hi:[1,0]
	v_mov_b32_e32 v22, v1
	v_mov_b32_e32 v23, v1
	v_pk_mul_f32 v[32:33], v[172:173], v[32:33]
	v_pk_mul_f32 v[46:47], v[176:177], v[50:51]
	v_pk_mul_f32 v[44:45], v[174:175], v[52:53]
	v_pk_mul_f32 v[48:49], v[178:179], v[54:55]
	v_mul_f32_e32 v41, 0x42000000, v32
	v_mul_f32_e32 v50, 0x42000000, v33
	v_mul_f32_e32 v53, 0x42000000, v46
	v_mul_f32_e32 v54, 0x42000000, v47
	v_mul_f32_e32 v51, 0x42000000, v44
	v_mul_f32_e32 v52, 0x42000000, v45
	v_mul_f32_e32 v55, 0x42000000, v48
	v_cvt_pk_bf16_f32 v42, v32, v33
	v_cvt_pk_bf16_f32 v43, v44, v45
	v_cvt_pk_bf16_f32 v44, v46, v47
	v_cvt_pk_bf16_f32 v45, v48, v49
	v_med3_f32 v32, v41, s76, v237
	v_med3_f32 v33, v50, s76, v237
	v_med3_f32 v47, v53, s76, v237
	v_med3_f32 v48, v54, s76, v237
	v_cvt_pk_fp8_f32 v22, v32, v33
	v_cvt_pk_fp8_f32 v23, v47, v48
	v_mul_f32_e32 v56, 0x42000000, v49
	v_med3_f32 v41, v51, s76, v237
	v_med3_f32 v46, v52, s76, v237
	v_med3_f32 v49, v55, s76, v237
	v_med3_f32 v50, v56, s76, v237
	v_cvt_pk_fp8_f32 v22, v41, v46 op_sel:[0,0,1]
	v_cvt_pk_fp8_f32 v23, v49, v50 op_sel:[0,0,1]
	global_store_dwordx2 v[20:21], v[22:23], off offset:1024
	global_store_dwordx4 v[18:19], v[42:45], off offset:2048
	v_pk_mul_f32 v[22:23], v[26:27], v[0:1] op_sel_hi:[1,0]
	v_pk_mul_f32 v[26:27], v[30:31], v[0:1] op_sel_hi:[1,0]
	v_mov_b32_e32 v32, v1
	v_mov_b32_e32 v33, v1
	v_pk_mul_f32 v[22:23], v[22:23], v[180:181]
	v_pk_mul_f32 v[26:27], v[26:27], v[184:185]
	v_pk_mul_f32 v[24:25], v[24:25], v[182:183]
	v_mul_f32_e32 v0, 0x42000000, v22
	v_mul_f32_e32 v30, 0x42000000, v23
	v_mul_f32_e32 v31, 0x42000000, v24
	v_mul_f32_e32 v41, 0x42000000, v25
	v_mul_f32_e32 v42, 0x42000000, v26
	v_mul_f32_e32 v43, 0x42000000, v27
	v_cvt_pk_bf16_f32 v22, v22, v23
	v_cvt_pk_bf16_f32 v23, v24, v25
	v_med3_f32 v0, v0, s76, v237
	v_med3_f32 v24, v30, s76, v237
	v_med3_f32 v25, v31, s76, v237
	v_med3_f32 v30, v41, s76, v237
	v_med3_f32 v31, v42, s76, v237
	v_med3_f32 v41, v43, s76, v237
	v_cvt_pk_fp8_f32 v32, v0, v24
	v_cvt_pk_fp8_f32 v33, v31, v41
	v_pk_mul_f32 v[28:29], v[28:29], v[186:187]
	v_cvt_pk_bf16_f32 v24, v26, v27
	v_mul_f32_e32 v44, 0x42000000, v28
	v_mul_f32_e32 v45, 0x42000000, v29
	v_med3_f32 v42, v44, s76, v237
	v_med3_f32 v0, v45, s76, v237
	v_cvt_pk_fp8_f32 v32, v25, v30 op_sel:[0,0,1]
	v_cvt_pk_fp8_f32 v33, v42, v0 op_sel:[0,0,1]
	v_cvt_pk_bf16_f32 v25, v28, v29
	global_store_dwordx2 v[20:21], v[32:33], off offset:1536
	global_store_dwordx4 v[18:19], v[22:25], off offset:3072
	s_cbranch_scc0 .LBB0_2271

.LBB0_7074:
	s_lshl_b32 s0, s43, 3
	s_add_i32 s2, s6, s0
	s_cmpk_gt_i32 s2, 0x3fff
	s_waitcnt vmcnt(0) lgkmcnt(0)
	s_barrier
	s_cbranch_scc1 .LBB0_7077
	v_xor_b32_e32 v1, 1, v218
	v_cmp_lt_i32_e32 vcc, v1, v219
	s_load_dwordx4 s[4:7], s[10:11], 0x110
	v_lshlrev_b32_e32 v44, 5, v0
	v_cndmask_b32_e32 v1, v218, v1, vcc
	v_lshlrev_b32_e32 v74, 2, v1
	v_xor_b32_e32 v1, 2, v218
	v_cmp_lt_i32_e32 vcc, v1, v219
	v_mov_b32_e32 v45, 0
	v_or_b32_e32 v2, 0x1000, v44
	v_cndmask_b32_e32 v1, v218, v1, vcc
	v_lshlrev_b32_e32 v75, 2, v1
	v_xor_b32_e32 v1, 4, v218
	v_cmp_lt_i32_e32 vcc, v1, v219
	v_mov_b32_e32 v3, v45
	s_waitcnt lgkmcnt(0)
	v_lshl_add_u64 v[48:49], s[4:5], 0, v[2:3]
	v_cndmask_b32_e32 v1, v218, v1, vcc
	v_lshlrev_b32_e32 v76, 2, v1
	v_xor_b32_e32 v1, 8, v218
	v_cmp_lt_i32_e32 vcc, v1, v219
	v_or_b32_e32 v2, 0x1800, v44
	v_lshl_add_u64 v[50:51], s[4:5], 0, v[2:3]
	v_cndmask_b32_e32 v1, v218, v1, vcc
	v_lshlrev_b32_e32 v77, 2, v1
	v_xor_b32_e32 v1, 16, v218
	v_lshlrev_b32_e32 v2, 4, v0
	v_cmp_lt_i32_e32 vcc, v1, v219
	v_lshl_add_u64 v[2:3], s[8:9], 0, v[2:3]
	s_mov_b64 s[0:1], 0x22600000
	s_ashr_i32 s3, s2, 31
	v_cndmask_b32_e32 v1, v218, v1, vcc
	v_lshl_add_u64 v[52:53], v[2:3], 0, s[0:1]
	s_lshl_b64 s[0:1], s[2:3], 12
	v_lshlrev_b32_e32 v78, 2, v1
	v_xor_b32_e32 v1, 32, v218
	v_lshl_add_u64 v[46:47], s[4:5], 0, v[44:45]
	v_lshl_or_b32 v54, v0, 4, s0
	v_mov_b32_e32 v55, s1
	s_lshl_b64 s[0:1], s[2:3], 4
	s_lshl_b64 s[4:5], s[2:3], 13
	v_cmp_lt_i32_e32 vcc, v1, v219
	s_add_u32 s4, s6, s4
	s_addc_u32 s5, s7, s5
	v_cndmask_b32_e32 v1, v218, v1, vcc
	v_lshlrev_b32_e32 v79, 2, v1
	v_lshl_add_u64 v[0:1], s[4:5], 0, v[44:45]
	s_mov_b64 s[4:5], 0x1000
	v_lshl_add_u64 v[56:57], v[0:1], 0, s[4:5]
	s_lshl_b64 s[4:5], s[2:3], 3
	s_add_u32 s3, s4, 0x15d80000
	s_addc_u32 s4, s5, 0
	v_mov_b32_e32 v44, 0x15d00000
	s_add_i32 s5, 0, 0x20200
	s_mov_b32 s6, 0x15e00000
	v_mov_b32_e32 v80, 0x358637bd
	s_mov_b32 s7, 0x800000
	v_readlane_b32 s16, v254, 29
	v_readlane_b32 s17, v254, 30
	s_add_u32 s98, s8, s0
	s_addc_u32 s99, s9, s1
	global_load_dwordx4 v[188:191], v44, s[98:99]
	global_load_dwordx4 v[156:159], v[46:47], off offset:16
	global_load_dwordx4 v[160:163], v[46:47], off
	global_load_dwordx4 v[164:167], v[46:47], off offset:2048
	global_load_dwordx4 v[168:171], v[46:47], off offset:2064
	global_load_dwordx4 v[172:175], v[48:49], off
	global_load_dwordx4 v[176:179], v[48:49], off offset:16
	global_load_dwordx4 v[180:183], v[50:51], off
	global_load_dwordx4 v[184:187], v[50:51], off offset:16
	s_waitcnt vmcnt(0)
.LBB0_7076:
	v_lshl_add_u64 v[0:1], s[8:9], 0, v[54:55]
	v_add_co_u32_e32 v8, vcc, s6, v0
	v_lshl_add_u64 v[54:55], v[54:55], 0, s[74:75]
	s_nop 0
	v_addc_co_u32_e32 v9, vcc, 0, v1, vcc
	s_add_u32 s10, s8, s3
	s_addc_u32 s11, s9, s4
	s_add_i32 s2, s2, s16
	v_readfirstlane_b32 s12, v188
	v_readfirstlane_b32 s14, v190
	s_lshl_b32 s12, s12, 2
	s_lshl_b32 s14, s14, 2
	s_add_i32 s12, s5, s12
	s_add_i32 s14, s5, s14
	v_mov_b32_e32 v0, s12
	v_readfirstlane_b32 s13, v189
	v_mov_b32_e32 v1, s14
	ds_read_b32 v10, v0
	ds_read_b32 v11, v1
	v_readfirstlane_b32 s15, v191
	s_add_u32 s98, s0, s80
	s_addc_u32 s99, s1, s81
	s_add_u32 s98, s98, s8
	s_addc_u32 s99, s99, s9
	global_load_dwordx4 v[188:191], v44, s[98:99]
	global_load_dwordx4 v[66:69], v[8:9], off
	global_load_dwordx4 v[82:85], v[8:9], off offset:1024
	global_load_dwordx4 v[86:89], v[8:9], off offset:2048
	global_load_dwordx4 v[32:35], v[8:9], off offset:3072
	global_load_dwordx2 v[58:59], v45, s[10:11]
	s_waitcnt lgkmcnt(1)
	v_readfirstlane_b32 s10, v10
	s_waitcnt lgkmcnt(0)
	v_readfirstlane_b32 s11, v11
	s_lshl_b32 s11, s11, 8
	s_lshl_b32 s10, s10, 8
	s_add_i32 s12, s11, s15
	s_add_i32 s10, s10, s13
	s_ashr_i32 s13, s12, 31
	s_ashr_i32 s11, s10, 31
	s_lshl_b64 s[12:13], s[12:13], 12
	s_lshl_b64 s[10:11], s[10:11], 12
	v_lshl_add_u64 v[62:63], v[52:53], 0, s[12:13]
	v_lshl_add_u64 v[60:61], v[52:53], 0, s[10:11]
	global_load_dwordx4 v[36:39], v[62:63], off
	global_load_dwordx4 v[40:43], v[60:61], off
	global_load_dwordx4 v[24:27], v[62:63], off offset:1024
	global_load_dwordx4 v[28:31], v[60:61], off offset:1024
	global_load_dwordx4 v[16:19], v[62:63], off offset:2048
	global_load_dwordx4 v[20:23], v[60:61], off offset:2048
	global_load_dwordx4 v[8:11], v[60:61], off offset:3072
	global_load_dwordx4 v[12:15], v[62:63], off offset:3072
	s_add_u32 s0, s0, s80
	s_addc_u32 s1, s1, s81
	s_add_u32 s3, s3, s84
	s_addc_u32 s4, s4, s85
	s_cmpk_lt_i32 s2, 0x4000
	s_waitcnt vmcnt(12)
	v_lshlrev_b32_e32 v64, 16, v66
	v_and_b32_e32 v65, 0xffff0000, v66
	v_lshlrev_b32_e32 v66, 16, v67
	v_and_b32_e32 v67, 0xffff0000, v67
	v_lshlrev_b32_e32 v60, 16, v68
	v_and_b32_e32 v61, 0xffff0000, v68
	v_lshlrev_b32_e32 v62, 16, v69
	v_and_b32_e32 v63, 0xffff0000, v69
	s_waitcnt vmcnt(9)
	v_lshlrev_b32_e32 v94, 16, v32
	v_and_b32_e32 v95, 0xffff0000, v32
	v_lshlrev_b32_e32 v32, 16, v33
	v_and_b32_e32 v33, 0xffff0000, v33
	v_lshlrev_b32_e32 v72, 16, v82
	s_waitcnt vmcnt(7)
	v_and_b32_e32 v99, 0xffff0000, v38
	s_waitcnt vmcnt(6)
	v_and_b32_e32 v97, 0xffff0000, v42
	v_lshlrev_b32_e32 v98, 16, v42
	v_lshlrev_b32_e32 v42, 16, v36
	v_lshlrev_b32_e32 v102, 16, v40
	v_and_b32_e32 v103, 0xffff0000, v36
	v_lshlrev_b32_e32 v104, 16, v37
	v_lshlrev_b32_e32 v36, 16, v41
	v_and_b32_e32 v37, 0xffff0000, v37
	v_lshlrev_b32_e32 v96, 16, v38
	v_and_b32_e32 v101, 0xffff0000, v43
	v_lshlrev_b32_e32 v38, 16, v43
	v_and_b32_e32 v43, 0xffff0000, v40
	v_and_b32_e32 v105, 0xffff0000, v41
	s_waitcnt vmcnt(5)
	v_lshlrev_b32_e32 v40, 16, v26
	s_waitcnt vmcnt(4)
	v_and_b32_e32 v41, 0xffff0000, v30
	v_lshlrev_b32_e32 v106, 16, v30
	v_and_b32_e32 v107, 0xffff0000, v26
	v_and_b32_e32 v109, 0xffff0000, v31
	v_lshlrev_b32_e32 v26, 16, v31
	v_lshlrev_b32_e32 v30, 16, v24
	v_and_b32_e32 v31, 0xffff0000, v28
	v_lshlrev_b32_e32 v110, 16, v28
	v_and_b32_e32 v111, 0xffff0000, v24
	v_and_b32_e32 v113, 0xffff0000, v29
	v_lshlrev_b32_e32 v24, 16, v29
	s_waitcnt vmcnt(3)
	v_lshlrev_b32_e32 v28, 16, v18
	s_waitcnt vmcnt(2)
	v_and_b32_e32 v29, 0xffff0000, v22
	v_lshlrev_b32_e32 v114, 16, v22
	v_and_b32_e32 v115, 0xffff0000, v18
	v_and_b32_e32 v117, 0xffff0000, v23
	v_lshlrev_b32_e32 v18, 16, v23
	v_lshlrev_b32_e32 v22, 16, v16
	v_and_b32_e32 v23, 0xffff0000, v20
	v_lshlrev_b32_e32 v118, 16, v20
	v_and_b32_e32 v119, 0xffff0000, v16
	v_and_b32_e32 v121, 0xffff0000, v21
	v_lshlrev_b32_e32 v16, 16, v21
	s_waitcnt vmcnt(0)
	v_lshlrev_b32_e32 v20, 16, v14
	v_and_b32_e32 v21, 0xffff0000, v10
	v_lshlrev_b32_e32 v122, 16, v10
	v_and_b32_e32 v123, 0xffff0000, v14
	v_lshlrev_b32_e32 v124, 16, v15
	v_and_b32_e32 v125, 0xffff0000, v11
	v_lshlrev_b32_e32 v10, 16, v11
	v_and_b32_e32 v11, 0xffff0000, v15
	v_lshlrev_b32_e32 v14, 16, v12
	v_and_b32_e32 v15, 0xffff0000, v8
	v_lshlrev_b32_e32 v126, 16, v8
	v_and_b32_e32 v127, 0xffff0000, v12
	v_lshlrev_b32_e32 v128, 16, v13
	v_and_b32_e32 v129, 0xffff0000, v9
	v_lshlrev_b32_e32 v8, 16, v9
	v_and_b32_e32 v9, 0xffff0000, v13
	v_pk_mul_f32 v[12:13], v[58:59], v[98:99]
	v_pk_mul_f32 v[98:99], v[58:59], v[102:103]
	v_pk_mul_f32 v[36:37], v[58:59], v[36:37]
	v_lshlrev_b32_e32 v100, 16, v39
	v_and_b32_e32 v39, 0xffff0000, v39
	v_lshlrev_b32_e32 v108, 16, v27
	v_and_b32_e32 v27, 0xffff0000, v27
	v_lshlrev_b32_e32 v112, 16, v25
	v_and_b32_e32 v25, 0xffff0000, v25
	v_lshlrev_b32_e32 v116, 16, v19
	v_and_b32_e32 v19, 0xffff0000, v19
	v_lshlrev_b32_e32 v120, 16, v17
	v_and_b32_e32 v17, 0xffff0000, v17
	v_pk_fma_f32 v[42:43], v[58:59], v[42:43], v[98:99] op_sel:[1,0,0] op_sel_hi:[0,1,1]
	v_pk_fma_f32 v[36:37], v[58:59], v[104:105], v[36:37] op_sel:[1,0,0] op_sel_hi:[0,1,1]
	v_pk_mul_f32 v[38:39], v[58:59], v[38:39]
	v_pk_mul_f32 v[102:103], v[58:59], v[106:107]
	v_pk_mul_f32 v[26:27], v[58:59], v[26:27]
	v_pk_mul_f32 v[106:107], v[58:59], v[110:111]
	v_pk_mul_f32 v[24:25], v[58:59], v[24:25]
	v_pk_mul_f32 v[110:111], v[58:59], v[114:115]
	v_pk_mul_f32 v[18:19], v[58:59], v[18:19]
	v_pk_mul_f32 v[114:115], v[58:59], v[118:119]
	v_pk_mul_f32 v[16:17], v[58:59], v[16:17]
	v_pk_mul_f32 v[118:119], v[58:59], v[122:123]
	v_pk_mul_f32 v[10:11], v[58:59], v[10:11]
	v_pk_mul_f32 v[122:123], v[58:59], v[126:127]
	v_pk_mul_f32 v[8:9], v[58:59], v[8:9]
	v_pk_fma_f32 v[12:13], v[58:59], v[96:97], v[12:13] op_sel:[1,0,0] op_sel_hi:[0,1,1]
	v_pk_add_f32 v[42:43], v[42:43], v[64:65]
	v_pk_add_f32 v[36:37], v[36:37], v[66:67]
	v_pk_fma_f32 v[38:39], v[58:59], v[100:101], v[38:39] op_sel:[1,0,0] op_sel_hi:[0,1,1]
	v_pk_fma_f32 v[40:41], v[58:59], v[40:41], v[102:103] op_sel:[1,0,0] op_sel_hi:[0,1,1]
	v_pk_fma_f32 v[26:27], v[58:59], v[108:109], v[26:27] op_sel:[1,0,0] op_sel_hi:[0,1,1]
	v_pk_fma_f32 v[30:31], v[58:59], v[30:31], v[106:107] op_sel:[1,0,0] op_sel_hi:[0,1,1]
	v_pk_fma_f32 v[24:25], v[58:59], v[112:113], v[24:25] op_sel:[1,0,0] op_sel_hi:[0,1,1]
	v_pk_fma_f32 v[28:29], v[58:59], v[28:29], v[110:111] op_sel:[1,0,0] op_sel_hi:[0,1,1]
	v_pk_fma_f32 v[18:19], v[58:59], v[116:117], v[18:19] op_sel:[1,0,0] op_sel_hi:[0,1,1]
	v_pk_fma_f32 v[22:23], v[58:59], v[22:23], v[114:115] op_sel:[1,0,0] op_sel_hi:[0,1,1]
	v_pk_fma_f32 v[16:17], v[58:59], v[120:121], v[16:17] op_sel:[1,0,0] op_sel_hi:[0,1,1]
	v_pk_fma_f32 v[20:21], v[58:59], v[20:21], v[118:119] op_sel:[1,0,0] op_sel_hi:[0,1,1]
	v_pk_fma_f32 v[10:11], v[58:59], v[124:125], v[10:11] op_sel:[1,0,0] op_sel_hi:[0,1,1]
	v_pk_fma_f32 v[14:15], v[58:59], v[14:15], v[122:123] op_sel:[1,0,0] op_sel_hi:[0,1,1]
	v_pk_fma_f32 v[8:9], v[58:59], v[128:129], v[8:9] op_sel:[1,0,0] op_sel_hi:[0,1,1]
	v_pk_add_f32 v[12:13], v[12:13], v[60:61]
	v_pk_mul_f32 v[58:59], v[42:43], v[42:43]
	v_pk_mul_f32 v[60:61], v[36:37], v[36:37]
	v_and_b32_e32 v73, 0xffff0000, v82
	v_lshlrev_b32_e32 v92, 16, v34
	v_and_b32_e32 v93, 0xffff0000, v34
	v_lshlrev_b32_e32 v34, 16, v35
	v_and_b32_e32 v35, 0xffff0000, v35
	v_pk_add_f32 v[38:39], v[38:39], v[62:63]
	v_pk_add_f32 v[8:9], v[8:9], v[32:33]
	v_pk_mul_f32 v[32:33], v[12:13], v[12:13]
	v_add_f32_e32 v60, v60, v61
	v_add_f32_e32 v58, v58, v59
	v_lshlrev_b32_e32 v82, 16, v83
	v_and_b32_e32 v83, 0xffff0000, v83
	v_pk_add_f32 v[30:31], v[30:31], v[72:73]
	v_pk_add_f32 v[10:11], v[10:11], v[34:35]
	v_pk_mul_f32 v[34:35], v[38:39], v[38:39]
	v_add_f32_e32 v59, v32, v33
	v_add_f32_e32 v58, v58, v60
	v_lshlrev_b32_e32 v68, 16, v84
	v_and_b32_e32 v69, 0xffff0000, v84
	v_pk_add_f32 v[24:25], v[24:25], v[82:83]
	v_pk_mul_f32 v[66:67], v[30:31], v[30:31]
	v_add_f32_e32 v81, v34, v35
	v_add_f32_e32 v58, v59, v58
	v_lshlrev_b32_e32 v70, 16, v85
	v_and_b32_e32 v71, 0xffff0000, v85
	v_pk_add_f32 v[40:41], v[40:41], v[68:69]
	v_pk_mul_f32 v[68:69], v[24:25], v[24:25]
	v_add_f32_e32 v61, v66, v67
	v_add_f32_e32 v58, v81, v58
	v_lshlrev_b32_e32 v90, 16, v86
	v_and_b32_e32 v91, 0xffff0000, v86
	v_pk_add_f32 v[26:27], v[26:27], v[70:71]
	v_pk_mul_f32 v[62:63], v[40:41], v[40:41]
	v_add_f32_e32 v66, v68, v69
	v_add_f32_e32 v58, v58, v61
	v_lshlrev_b32_e32 v86, 16, v87
	v_and_b32_e32 v87, 0xffff0000, v87
	v_pk_add_f32 v[22:23], v[22:23], v[90:91]
	v_pk_mul_f32 v[64:65], v[26:27], v[26:27]
	v_add_f32_e32 v62, v62, v63
	v_add_f32_e32 v58, v66, v58
	v_lshlrev_b32_e32 v84, 16, v88
	v_and_b32_e32 v85, 0xffff0000, v88
	v_pk_add_f32 v[16:17], v[16:17], v[86:87]
	v_pk_mul_f32 v[82:83], v[22:23], v[22:23]
	v_add_f32_e32 v63, v64, v65
	v_add_f32_e32 v58, v62, v58
	v_lshlrev_b32_e32 v88, 16, v89
	v_and_b32_e32 v89, 0xffff0000, v89
	v_pk_add_f32 v[28:29], v[28:29], v[84:85]
	v_pk_mul_f32 v[84:85], v[16:17], v[16:17]
	v_add_f32_e32 v64, v82, v83
	v_add_f32_e32 v58, v63, v58
	v_pk_add_f32 v[18:19], v[18:19], v[88:89]
	v_pk_add_f32 v[14:15], v[14:15], v[94:95]
	v_pk_mul_f32 v[70:71], v[28:29], v[28:29]
	v_add_f32_e32 v65, v84, v85
	v_add_f32_e32 v58, v64, v58
	v_pk_add_f32 v[20:21], v[20:21], v[92:93]
	v_pk_mul_f32 v[72:73], v[18:19], v[18:19]
	v_mov_b32_e32 v92, v9
	v_mov_b32_e32 v93, v15
	v_add_f32_e32 v67, v70, v71
	v_add_f32_e32 v58, v65, v58
	v_mov_b32_e32 v90, v8
	v_mov_b32_e32 v91, v14
	v_pk_mul_f32 v[92:93], v[92:93], v[92:93]
	v_add_f32_e32 v68, v72, v73
	v_add_f32_e32 v58, v67, v58
	v_mov_b32_e32 v88, v11
	v_mov_b32_e32 v89, v21
	v_pk_fma_f32 v[34:35], v[90:91], v[90:91], v[92:93]
	v_add_f32_e32 v58, v68, v58
	v_mov_b32_e32 v86, v10
	v_mov_b32_e32 v87, v20
	v_pk_mul_f32 v[88:89], v[88:89], v[88:89]
	v_add_f32_e32 v35, v35, v58
	v_pk_fma_f32 v[32:33], v[86:87], v[86:87], v[88:89]
	v_add_f32_e32 v34, v34, v35
	v_add_f32_e32 v33, v33, v34
	v_add_f32_e32 v32, v32, v33
	ds_bpermute_b32 v33, v74, v32
	s_waitcnt lgkmcnt(0)
	v_add_f32_e32 v32, v32, v33
	ds_bpermute_b32 v33, v75, v32
	s_waitcnt lgkmcnt(0)
	v_add_f32_e32 v32, v32, v33
	ds_bpermute_b32 v33, v76, v32
	s_waitcnt lgkmcnt(0)
	v_add_f32_e32 v32, v32, v33
	ds_bpermute_b32 v33, v77, v32
	s_waitcnt lgkmcnt(0)
	v_add_f32_e32 v32, v32, v33
	ds_bpermute_b32 v33, v78, v32
	s_waitcnt lgkmcnt(0)
	v_add_f32_e32 v32, v32, v33
	ds_bpermute_b32 v33, v79, v32
	s_waitcnt lgkmcnt(0)
	v_add_f32_e32 v32, v32, v33
	v_fmamk_f32 v32, v32, 0x3a000000, v80
	v_mul_f32_e32 v33, 0x4b800000, v32
	v_cmp_gt_f32_e32 vcc, s7, v32
	s_nop 1
	v_cndmask_b32_e32 v32, v32, v33, vcc
	v_rsq_f32_e32 v32, v32
	s_nop 0
	v_mul_f32_e32 v33, 0x45800000, v32
	v_cndmask_b32_e32 v32, v32, v33, vcc
	v_pk_mul_f32 v[34:35], v[42:43], v[32:33] op_sel_hi:[1,0]
	v_pk_mul_f32 v[36:37], v[36:37], v[32:33] op_sel_hi:[1,0]
	v_pk_mul_f32 v[12:13], v[12:13], v[32:33] op_sel_hi:[1,0]
	v_pk_mul_f32 v[38:39], v[38:39], v[32:33] op_sel_hi:[1,0]
	v_pk_mul_f32 v[6:7], v[162:163], v[36:37]
	v_pk_mul_f32 v[4:5], v[160:161], v[34:35]
	v_pk_mul_f32 v[2:3], v[158:159], v[38:39]
	v_pk_mul_f32 v[0:1], v[156:157], v[12:13]
	global_store_dwordx4 v[56:57], v[4:7], off offset:-4096 nt
	global_store_dwordx4 v[56:57], v[0:3], off offset:-4080 nt
	v_pk_mul_f32 v[12:13], v[24:25], v[32:33] op_sel_hi:[1,0]
	v_pk_mul_f32 v[24:25], v[30:31], v[32:33] op_sel_hi:[1,0]
	v_pk_mul_f32 v[26:27], v[26:27], v[32:33] op_sel_hi:[1,0]
	v_pk_mul_f32 v[30:31], v[40:41], v[32:33] op_sel_hi:[1,0]
	v_pk_mul_f32 v[18:19], v[18:19], v[32:33] op_sel_hi:[1,0]
	v_pk_mul_f32 v[8:9], v[8:9], v[32:33] op_sel_hi:[1,0]
	v_pk_mul_f32 v[10:11], v[10:11], v[32:33] op_sel_hi:[1,0]
	v_pk_mul_f32 v[0:1], v[164:165], v[24:25]
	v_pk_mul_f32 v[2:3], v[166:167], v[12:13]
	v_pk_mul_f32 v[4:5], v[168:169], v[30:31]
	v_pk_mul_f32 v[6:7], v[170:171], v[26:27]
	global_store_dwordx4 v[56:57], v[0:3], off offset:-2048 nt
	global_store_dwordx4 v[56:57], v[4:7], off offset:-2032 nt
	v_pk_mul_f32 v[12:13], v[16:17], v[32:33] op_sel_hi:[1,0]
	v_pk_mul_f32 v[16:17], v[22:23], v[32:33] op_sel_hi:[1,0]
	v_pk_mul_f32 v[22:23], v[28:29], v[32:33] op_sel_hi:[1,0]
	v_pk_mul_f32 v[0:1], v[172:173], v[16:17]
	v_pk_mul_f32 v[2:3], v[174:175], v[12:13]
	v_pk_mul_f32 v[4:5], v[176:177], v[22:23]
	v_pk_mul_f32 v[6:7], v[178:179], v[18:19]
	global_store_dwordx4 v[56:57], v[0:3], off nt
	global_store_dwordx4 v[56:57], v[4:7], off offset:16 nt
	v_pk_mul_f32 v[12:13], v[14:15], v[32:33] op_sel_hi:[1,0]
	v_pk_mul_f32 v[14:15], v[20:21], v[32:33] op_sel_hi:[1,0]
	v_pk_mul_f32 v[0:1], v[180:181], v[12:13]
	v_pk_mul_f32 v[2:3], v[182:183], v[8:9]
	v_pk_mul_f32 v[4:5], v[184:185], v[14:15]
	v_pk_mul_f32 v[6:7], v[186:187], v[10:11]
	global_store_dwordx4 v[56:57], v[0:3], off offset:2048 nt
	global_store_dwordx4 v[56:57], v[4:7], off offset:2064 nt
	v_lshl_add_u64 v[56:57], v[56:57], 0, s[86:87]
	s_cbranch_scc1 .LBB0_7076
